# P5: dead global-address arithmetic left behind by the LDS q tile / LDS parking deleted (stage-2 loop and rescale pass)
# baseline (speedup 1.0000x reference)
.LBB0_788:
	v_add_u32_e32 v141, 0, v84
	ds_read_b128 v[200:203], v141
	ds_read_b128 v[204:207], v141 offset:64
	s_waitcnt vmcnt(0)
	v_mov_b64_e32 v[210:211], v[70:71]
	v_mov_b64_e32 v[208:209], v[68:69]
	s_waitcnt vmcnt(2)
	v_mov_b64_e32 v[218:219], v[62:63]
	s_waitcnt lgkmcnt(1)
	v_mfma_f32_16x16x32_bf16 v[80:83], v[32:35], v[200:203], 0
	s_waitcnt vmcnt(1)
	v_mov_b64_e32 v[214:215], v[74:75]
	v_mov_b64_e32 v[216:217], v[60:61]
	s_cmp_lg_u32 s58, 0x38000
	v_mfma_f32_16x16x32_bf16 v[68:71], v[0:3], v[208:211], 0
	ds_read_b128 v[220:223], v141 offset:128
	ds_read_b128 v[224:227], v141 offset:192
	v_mov_b64_e32 v[212:213], v[72:73]
	s_waitcnt lgkmcnt(2)
	v_mfma_f32_16x16x32_bf16 v[60:63], v[48:51], v[204:207], v[80:83]
	s_cselect_b32 s96, s49, 0x70
	s_mul_i32 s32, s96, 0x110
	v_add_u32_e32 v243, s32, v242
	v_add_u32_e32 v141, 0, v137
	v_add_u32_e32 v143, 0x19c00, v141
	v_mfma_f32_16x16x32_bf16 v[72:75], v[4:7], v[216:219], v[68:71]
	v_add_u32_e32 v141, 0x19e00, v141
	s_nop 1
	s_waitcnt lgkmcnt(1)
	v_mfma_f32_16x16x32_bf16 v[228:231], v[40:43], v[220:223], v[60:63]
	ds_read_b128 v[68:71], v243
	s_nop 1
	ds_read_b128 v[60:63], v243 offset:64
	v_mfma_f32_16x16x32_bf16 v[232:235], v[8:11], v[212:215], v[72:75]
	s_nop 2
	ds_read_b128 v[72:75], v243 offset:128
	s_nop 0
	ds_read_b128 v[80:83], v243 offset:192
	ds_read_b32 v236, v143
	ds_read_b32 v238, v141
	v_mfma_f32_16x16x32_bf16 v[200:203], v[36:39], v[200:203], 0
	v_mfma_f32_16x16x32_bf16 v[208:211], v[16:19], v[208:211], 0
	v_mfma_f32_16x16x32_bf16 v[200:203], v[52:55], v[204:207], v[200:203]
	v_mfma_f32_16x16x32_bf16 v[204:207], v[20:23], v[216:219], v[208:211]
	s_waitcnt lgkmcnt(6)
	v_mfma_f32_16x16x32_bf16 v[228:231], v[44:47], v[224:227], v[228:231]
	s_waitcnt vmcnt(4)
	v_mfma_f32_16x16x32_bf16 v[232:235], v[12:15], v[76:79], v[232:235]
	v_mfma_f32_16x16x32_bf16 v[200:203], v[56:59], v[220:223], v[200:203]
	v_mfma_f32_16x16x32_bf16 v[204:207], v[24:27], v[212:215], v[204:207]
	s_waitcnt lgkmcnt(1)
	s_nop 4
	v_pk_fma_f32 v[230:231], v[236:237], v[234:235], v[230:231] op_sel_hi:[0,1,1]
	v_pk_fma_f32 v[228:229], v[236:237], v[232:233], v[228:229] op_sel_hi:[0,1,1]
	s_waitcnt lgkmcnt(0)
	v_pk_mul_f32 v[230:231], v[238:239], v[230:231] op_sel_hi:[0,1]
	v_mfma_f32_16x16x32_bf16 v[200:203], v[64:67], v[224:227], v[200:203]
	v_mul_f32_e64 v228, v238, v228
	v_mul_f32_e64 v229, v238, v229
	v_mul_f32_e32 v141, v229, v229
	v_mul_f32_e32 v143, v231, v231
	v_mfma_f32_16x16x32_bf16 v[76:79], v[28:31], v[76:79], v[204:207]
	v_fmac_f32_e32 v141, v228, v228
	v_fmac_f32_e32 v143, v230, v230
	v_and_b32_sdwa v208, v231, v198 dst_sel:DWORD dst_unused:UNUSED_PAD src0_sel:WORD_1 src1_sel:DWORD
	v_and_b32_sdwa v209, v229, v198 dst_sel:DWORD dst_unused:UNUSED_PAD src0_sel:WORD_1 src1_sel:DWORD
	v_add_f32_e32 v141, v141, v143
	v_and_b32_sdwa v143, v230, v198 dst_sel:DWORD dst_unused:UNUSED_PAD src0_sel:WORD_1 src1_sel:DWORD
	v_and_b32_sdwa v199, v228, v198 dst_sel:DWORD dst_unused:UNUSED_PAD src0_sel:WORD_1 src1_sel:DWORD
	v_add3_u32 v208, v231, v208, s71
	v_add3_u32 v209, v229, v209, s71
	v_pk_fma_f32 v[78:79], v[236:237], v[78:79], v[202:203] op_sel_hi:[0,1,1]
	v_pk_fma_f32 v[76:77], v[236:237], v[76:77], v[200:201] op_sel_hi:[0,1,1]
	v_add3_u32 v199, v228, v199, s71
	v_add3_u32 v143, v230, v143, s71
	v_and_b32_e32 v208, 0xffff0000, v208
	v_and_b32_e32 v210, 0xffff0000, v209
	v_pk_mul_f32 v[78:79], v[238:239], v[78:79] op_sel_hi:[0,1]
	v_pk_mul_f32 v[76:77], v[238:239], v[76:77] op_sel_hi:[0,1]
	v_or_b32_sdwa v209, v208, v143 dst_sel:DWORD dst_unused:UNUSED_PAD src0_sel:DWORD src1_sel:WORD_1
	v_or_b32_sdwa v208, v210, v199 dst_sel:DWORD dst_unused:UNUSED_PAD src0_sel:DWORD src1_sel:WORD_1
	v_mul_f32_e32 v143, v77, v77
	v_mul_f32_e32 v199, v79, v79
	v_fmac_f32_e32 v143, v76, v76
	v_fmac_f32_e32 v199, v78, v78
	v_add_f32_e32 v143, v143, v199
	v_add_f32_e32 v141, v141, v143
	v_and_b32_sdwa v143, v78, v198 dst_sel:DWORD dst_unused:UNUSED_PAD src0_sel:WORD_1 src1_sel:DWORD
	v_add3_u32 v78, v78, v143, s71
	ds_bpermute_b32 v143, v160, v141
	v_and_b32_sdwa v199, v76, v198 dst_sel:DWORD dst_unused:UNUSED_PAD src0_sel:WORD_1 src1_sel:DWORD
	v_add3_u32 v199, v76, v199, s71
	v_and_b32_sdwa v76, v79, v198 dst_sel:DWORD dst_unused:UNUSED_PAD src0_sel:WORD_1 src1_sel:DWORD
	v_and_b32_sdwa v200, v77, v198 dst_sel:DWORD dst_unused:UNUSED_PAD src0_sel:WORD_1 src1_sel:DWORD
	v_add3_u32 v76, v79, v76, s71
	v_add3_u32 v79, v77, v200, s71
	v_and_b32_e32 v200, 0xffff0000, v76
	s_waitcnt lgkmcnt(0)
	v_add_f32_e32 v76, v141, v143
	ds_bpermute_b32 v77, v161, v76
	v_and_b32_e32 v141, 0xffff0000, v79
	s_nop 0
	v_or_b32_sdwa v79, v200, v78 dst_sel:DWORD dst_unused:UNUSED_PAD src0_sel:DWORD src1_sel:WORD_1
	v_or_b32_sdwa v78, v141, v199 dst_sel:DWORD dst_unused:UNUSED_PAD src0_sel:DWORD src1_sel:WORD_1
	s_lshr_b32 s32, s58, 5
	v_add_u32_e32 v241, s32, v240
	ds_write_b64 v241, v[208:209]
	ds_write_b64 v241, v[78:79] offset:512
	s_and_saveexec_b64 s[60:61], s[10:11]
	s_cbranch_execz .LBB0_787
	v_add_u32_e32 v78, 0, v139
	s_waitcnt lgkmcnt(0)
	v_add_f32_e32 v76, v76, v77
	ds_write_b32 v78, v76
	s_branch .LBB0_787
.LBB0_790:
	s_lshl_b32 s96, s56, 1
	s_add_u32 s58, s42, s96
	s_addc_u32 s59, s43, 0
	v_mov_b32_e32 v143, v85
	v_mov_b64_e32 v[0:1], s[88:89]
	v_lshl_add_u64 v[10:11], s[58:59], 0, v[142:143]
	v_mad_u64_u32 v[0:1], s[58:59], v146, s65, v[0:1]
	v_mov_b32_e32 v2, v1
	v_mad_u64_u32 v[2:3], s[58:59], v147, s65, v[2:3]
	v_mov_b32_e32 v1, v2
	v_lshl_add_u64 v[0:1], v[0:1], 0, s[96:97]
	v_lshl_add_u64 v[0:1], v[0:1], 0, v[142:143]
	s_mov_b32 s49, s97
	v_lshl_add_u64 v[0:1], v[0:1], 0, s[48:49]
	v_lshl_add_u64 v[2:3], v[0:1], 0, s[50:51]
	v_add_co_u32_e32 v0, vcc, s73, v0
	s_lshl_b32 s56, s56, 2
	s_nop 0
	v_addc_co_u32_e32 v1, vcc, 0, v1, vcc
	global_load_dwordx2 v[22:23], v[0:1], off offset:2560
	global_load_dwordx2 v[16:17], v[2:3], off offset:32
	v_lshlrev_b64 v[0:1], 11, v[146:147]
	v_lshl_add_u64 v[0:1], s[42:43], 0, v[0:1]
	v_lshl_add_u64 v[0:1], v[0:1], 0, s[96:97]
	s_mov_b32 s57, s97
	v_lshl_add_u64 v[4:5], v[0:1], 0, v[142:143]
	v_lshl_add_u64 v[6:7], v[130:131], 0, s[56:57]
	global_load_dwordx4 v[0:3], v[6:7], off
	ds_read_b64 v[26:27], v240
	s_nop 0
	global_load_dwordx4 v[4:7], v[6:7], off offset:64
	s_nop 0
	ds_read_b64 v[24:25], v240 offset:512
	s_mov_b64 s[56:57], 0
	s_mov_b32 s53, 16
	v_mov_b32_e32 v29, v181
	s_movk_i32 s58, 0x10
	v_or_b32_e32 v84, s58, v86
	v_lshl_add_u64 v[12:13], s[54:55], 0, v[84:85]
	v_mov_b64_e32 v[14:15], s[88:89]
	v_mad_u64_u32 v[14:15], s[58:59], v12, s65, v[14:15]
	v_mov_b32_e32 v18, v15
	v_mad_u64_u32 v[18:19], s[58:59], v13, s65, v[18:19]
	v_mov_b32_e32 v15, v18
	v_lshl_add_u64 v[14:15], v[14:15], 0, s[96:97]
	v_lshl_add_u64 v[14:15], v[14:15], 0, v[142:143]
	v_lshl_add_u64 v[14:15], v[14:15], 0, s[48:49]
	v_lshl_add_u64 v[20:21], v[14:15], 0, s[50:51]
	v_add_co_u32_e32 v14, vcc, s73, v14
	s_nop 0
	s_nop 0
	v_addc_co_u32_e32 v15, vcc, 0, v15, vcc
	global_load_dwordx2 v[40:41], v[14:15], off offset:2560
	ds_read_b64 v[42:43], v240 offset:1024
	s_nop 0
	global_load_dwordx2 v[44:45], v[20:21], off offset:32
	s_nop 0
	ds_read_b64 v[46:47], v240 offset:1536
	s_movk_i32 s58, 0x20
	v_or_b32_e32 v84, s58, v86
	v_lshl_add_u64 v[12:13], s[54:55], 0, v[84:85]
	v_mov_b64_e32 v[14:15], s[88:89]
	v_mad_u64_u32 v[14:15], s[58:59], v12, s65, v[14:15]
	v_mov_b32_e32 v18, v15
	v_mad_u64_u32 v[18:19], s[58:59], v13, s65, v[18:19]
	v_mov_b32_e32 v15, v18
	v_lshl_add_u64 v[14:15], v[14:15], 0, s[96:97]
	v_lshl_add_u64 v[14:15], v[14:15], 0, v[142:143]
	v_lshl_add_u64 v[14:15], v[14:15], 0, s[48:49]
	v_lshl_add_u64 v[20:21], v[14:15], 0, s[50:51]
	v_add_co_u32_e32 v14, vcc, s73, v14
	s_nop 0
	s_nop 0
	v_addc_co_u32_e32 v15, vcc, 0, v15, vcc
	global_load_dwordx2 v[48:49], v[14:15], off offset:2560
	ds_read_b64 v[50:51], v240 offset:2048
	s_nop 0
	global_load_dwordx2 v[52:53], v[20:21], off offset:32
	s_nop 0
	ds_read_b64 v[54:55], v240 offset:2560
	s_movk_i32 s58, 0x30
	v_or_b32_e32 v84, s58, v86
	v_lshl_add_u64 v[12:13], s[54:55], 0, v[84:85]
	v_mov_b64_e32 v[14:15], s[88:89]
	v_mad_u64_u32 v[14:15], s[58:59], v12, s65, v[14:15]
	v_mov_b32_e32 v18, v15
	v_mad_u64_u32 v[18:19], s[58:59], v13, s65, v[18:19]
	v_mov_b32_e32 v15, v18
	v_lshl_add_u64 v[14:15], v[14:15], 0, s[96:97]
	v_lshl_add_u64 v[14:15], v[14:15], 0, v[142:143]
	v_lshl_add_u64 v[14:15], v[14:15], 0, s[48:49]
	v_lshl_add_u64 v[20:21], v[14:15], 0, s[50:51]
	v_add_co_u32_e32 v14, vcc, s73, v14
	s_nop 0
	s_nop 0
	v_addc_co_u32_e32 v15, vcc, 0, v15, vcc
	global_load_dwordx2 v[56:57], v[14:15], off offset:2560
	ds_read_b64 v[58:59], v240 offset:3072
	s_nop 0
	global_load_dwordx2 v[60:61], v[20:21], off offset:32
	s_nop 0
	ds_read_b64 v[62:63], v240 offset:3584
	s_movk_i32 s58, 0x40
	v_or_b32_e32 v84, s58, v86
	v_lshl_add_u64 v[12:13], s[54:55], 0, v[84:85]
	v_mov_b64_e32 v[14:15], s[88:89]
	v_mad_u64_u32 v[14:15], s[58:59], v12, s65, v[14:15]
	v_mov_b32_e32 v18, v15
	v_mad_u64_u32 v[18:19], s[58:59], v13, s65, v[18:19]
	v_mov_b32_e32 v15, v18
	v_lshl_add_u64 v[14:15], v[14:15], 0, s[96:97]
	v_lshl_add_u64 v[14:15], v[14:15], 0, v[142:143]
	v_lshl_add_u64 v[14:15], v[14:15], 0, s[48:49]
	v_lshl_add_u64 v[20:21], v[14:15], 0, s[50:51]
	v_add_co_u32_e32 v14, vcc, s73, v14
	s_nop 0
	s_nop 0
	v_addc_co_u32_e32 v15, vcc, 0, v15, vcc
	global_load_dwordx2 v[64:65], v[14:15], off offset:2560
	ds_read_b64 v[66:67], v240 offset:4096
	s_nop 0
	global_load_dwordx2 v[68:69], v[20:21], off offset:32
	s_nop 0
	ds_read_b64 v[70:71], v240 offset:4608
	s_movk_i32 s58, 0x50
	v_or_b32_e32 v84, s58, v86
	v_lshl_add_u64 v[12:13], s[54:55], 0, v[84:85]
	v_mov_b64_e32 v[14:15], s[88:89]
	v_mad_u64_u32 v[14:15], s[58:59], v12, s65, v[14:15]
	v_mov_b32_e32 v18, v15
	v_mad_u64_u32 v[18:19], s[58:59], v13, s65, v[18:19]
	v_mov_b32_e32 v15, v18
	v_lshl_add_u64 v[14:15], v[14:15], 0, s[96:97]
	v_lshl_add_u64 v[14:15], v[14:15], 0, v[142:143]
	v_lshl_add_u64 v[14:15], v[14:15], 0, s[48:49]
	v_lshl_add_u64 v[20:21], v[14:15], 0, s[50:51]
	v_add_co_u32_e32 v14, vcc, s73, v14
	s_nop 0
	s_nop 0
	v_addc_co_u32_e32 v15, vcc, 0, v15, vcc
	global_load_dwordx2 v[72:73], v[14:15], off offset:2560
	ds_read_b64 v[74:75], v240 offset:5120
	s_nop 0
	global_load_dwordx2 v[76:77], v[20:21], off offset:32
	s_nop 0
	ds_read_b64 v[78:79], v240 offset:5632
	s_movk_i32 s58, 0x60
	v_or_b32_e32 v84, s58, v86
	v_lshl_add_u64 v[12:13], s[54:55], 0, v[84:85]
	v_mov_b64_e32 v[14:15], s[88:89]
	v_mad_u64_u32 v[14:15], s[58:59], v12, s65, v[14:15]
	v_mov_b32_e32 v18, v15
	v_mad_u64_u32 v[18:19], s[58:59], v13, s65, v[18:19]
	v_mov_b32_e32 v15, v18
	v_lshl_add_u64 v[14:15], v[14:15], 0, s[96:97]
	v_lshl_add_u64 v[14:15], v[14:15], 0, v[142:143]
	v_lshl_add_u64 v[14:15], v[14:15], 0, s[48:49]
	v_lshl_add_u64 v[20:21], v[14:15], 0, s[50:51]
	v_add_co_u32_e32 v14, vcc, s73, v14
	s_nop 0
	s_nop 0
	v_addc_co_u32_e32 v15, vcc, 0, v15, vcc
	global_load_dwordx2 v[200:201], v[14:15], off offset:2560
	ds_read_b64 v[202:203], v240 offset:6144
	s_nop 0
	global_load_dwordx2 v[204:205], v[20:21], off offset:32
	s_nop 0
	ds_read_b64 v[206:207], v240 offset:6656
	s_movk_i32 s58, 0x70
	v_or_b32_e32 v84, s58, v86
	v_lshl_add_u64 v[12:13], s[54:55], 0, v[84:85]
	v_mov_b64_e32 v[14:15], s[88:89]
	v_mad_u64_u32 v[14:15], s[58:59], v12, s65, v[14:15]
	v_mov_b32_e32 v18, v15
	v_mad_u64_u32 v[18:19], s[58:59], v13, s65, v[18:19]
	v_mov_b32_e32 v15, v18
	v_lshl_add_u64 v[14:15], v[14:15], 0, s[96:97]
	v_lshl_add_u64 v[14:15], v[14:15], 0, v[142:143]
	v_lshl_add_u64 v[14:15], v[14:15], 0, s[48:49]
	v_lshl_add_u64 v[20:21], v[14:15], 0, s[50:51]
	v_add_co_u32_e32 v14, vcc, s73, v14
	s_nop 0
	s_nop 0
	v_addc_co_u32_e32 v15, vcc, 0, v15, vcc
	global_load_dwordx2 v[208:209], v[14:15], off offset:2560
	ds_read_b64 v[210:211], v240 offset:7168
	s_nop 0
	global_load_dwordx2 v[212:213], v[20:21], off offset:32
	s_nop 0
	ds_read_b64 v[214:215], v240 offset:7680
	s_barrier
	s_waitcnt vmcnt(15)
	v_mov_b32_e32 v8, v1
	v_mov_b32_e32 v9, v3
	v_mov_b32_e32 v1, v2
	s_waitcnt vmcnt(14)
	v_mov_b32_e32 v2, v5
	v_mov_b32_e32 v3, v7
	v_mov_b32_e32 v5, v6
	v_lshl_add_u64 v[6:7], v[10:11], 0, s[48:49]
	v_lshl_add_u64 v[10:11], v[134:135], 0, v[144:145]
	s_waitcnt vmcnt(14)
	v_add_u32_e32 v28, -16, v29
	ds_read_b128 v[30:33], v28
	ds_read_b128 v[34:37], v29
	s_mov_b32 s58, 0x800000
	s_waitcnt lgkmcnt(1)
	v_mov_b32_e32 v38, v31
	v_mov_b32_e32 v39, v32
	v_mov_b32_e32 v31, v33
	v_pk_add_f32 v[30:31], v[38:39], v[30:31]
	s_waitcnt lgkmcnt(0)
	v_mov_b32_e32 v32, v36
	v_mov_b32_e32 v33, v34
	v_mov_b32_e32 v34, v37
	v_pk_add_f32 v[32:33], v[32:33], v[34:35]
	v_add_f32_e32 v28, v30, v31
	v_add_f32_e32 v28, v28, v33
	v_add_f32_e32 v28, v32, v28
	v_fmamk_f32 v28, v28, 0x3b800000, v195
	v_cmp_gt_f32_e32 vcc, s58, v28
	v_mul_f32_e32 v30, 0x4b800000, v28
	v_lshlrev_b32_e32 v33, 16, v27
	v_cndmask_b32_e32 v28, v28, v30, vcc
	v_rsq_f32_e32 v28, v28
	v_lshlrev_b32_e32 v32, 16, v26
	v_and_b32_e32 v27, 0xffff0000, v27
	v_and_b32_e32 v26, 0xffff0000, v26
	v_mul_f32_e32 v30, 0x45800000, v28
	v_cndmask_b32_e32 v28, v28, v30, vcc
	v_pk_mul_f32 v[32:33], v[28:29], v[32:33] op_sel_hi:[0,1]
	v_pk_mul_f32 v[32:33], v[0:1], v[32:33]
	v_lshlrev_b32_e32 v35, 16, v23
	v_lshlrev_b32_e32 v34, 16, v22
	v_pk_mul_f32 v[26:27], v[28:29], v[26:27] op_sel_hi:[0,1]
	v_pk_mul_f32 v[32:33], v[32:33], v[34:35]
	v_pk_mul_f32 v[26:27], v[8:9], v[26:27]
	v_and_b32_e32 v23, 0xffff0000, v23
	v_and_b32_e32 v22, 0xffff0000, v22
	v_pk_mul_f32 v[22:23], v[26:27], v[22:23]
	v_and_b32_sdwa v27, v32, v198 dst_sel:DWORD dst_unused:UNUSED_PAD src0_sel:WORD_1 src1_sel:DWORD
	v_and_b32_sdwa v26, v33, v198 dst_sel:DWORD dst_unused:UNUSED_PAD src0_sel:WORD_1 src1_sel:DWORD
	v_add3_u32 v27, v32, v27, s71
	v_and_b32_sdwa v32, v23, v198 dst_sel:DWORD dst_unused:UNUSED_PAD src0_sel:WORD_1 src1_sel:DWORD
	v_add3_u32 v26, v33, v26, s71
	v_and_b32_sdwa v33, v22, v198 dst_sel:DWORD dst_unused:UNUSED_PAD src0_sel:WORD_1 src1_sel:DWORD
	v_add3_u32 v23, v23, v32, s71
	v_lshl_add_u64 v[30:31], v[10:11], 0, s[56:57]
	v_add3_u32 v22, v22, v33, s71
	v_and_b32_e32 v23, 0xffff0000, v23
	v_and_b32_e32 v22, 0xffff0000, v22
	v_or_b32_sdwa v23, v23, v26 dst_sel:DWORD dst_unused:UNUSED_PAD src0_sel:DWORD src1_sel:WORD_1
	v_add_co_u32_e32 v26, vcc, s72, v30
	v_or_b32_sdwa v22, v22, v27 dst_sel:DWORD dst_unused:UNUSED_PAD src0_sel:DWORD src1_sel:WORD_1
	s_nop 0
	v_addc_co_u32_e32 v27, vcc, 0, v31, vcc
	global_store_dwordx2 v[26:27], v[22:23], off offset:3072
	v_lshlrev_b32_e32 v23, 16, v25
	v_lshlrev_b32_e32 v22, 16, v24
	v_pk_mul_f32 v[22:23], v[28:29], v[22:23] op_sel_hi:[0,1]
	v_and_b32_e32 v25, 0xffff0000, v25
	v_and_b32_e32 v24, 0xffff0000, v24
	v_pk_mul_f32 v[22:23], v[4:5], v[22:23]
	v_lshlrev_b32_e32 v31, 16, v17
	v_lshlrev_b32_e32 v30, 16, v16
	v_pk_mul_f32 v[24:25], v[28:29], v[24:25] op_sel_hi:[0,1]
	v_pk_mul_f32 v[22:23], v[22:23], v[30:31]
	v_pk_mul_f32 v[24:25], v[2:3], v[24:25]
	v_and_b32_e32 v17, 0xffff0000, v17
	v_and_b32_e32 v16, 0xffff0000, v16
	v_pk_mul_f32 v[16:17], v[24:25], v[16:17]
	v_and_b32_sdwa v24, v23, v198 dst_sel:DWORD dst_unused:UNUSED_PAD src0_sel:WORD_1 src1_sel:DWORD
	v_and_b32_sdwa v25, v22, v198 dst_sel:DWORD dst_unused:UNUSED_PAD src0_sel:WORD_1 src1_sel:DWORD
	v_add3_u32 v22, v22, v25, s71
	v_add3_u32 v23, v23, v24, s71
	v_and_b32_sdwa v24, v17, v198 dst_sel:DWORD dst_unused:UNUSED_PAD src0_sel:WORD_1 src1_sel:DWORD
	v_and_b32_sdwa v25, v16, v198 dst_sel:DWORD dst_unused:UNUSED_PAD src0_sel:WORD_1 src1_sel:DWORD
	v_add3_u32 v17, v17, v24, s71
	v_add3_u32 v16, v16, v25, s71
	v_and_b32_e32 v17, 0xffff0000, v17
	v_and_b32_e32 v16, 0xffff0000, v16
	s_add_u32 s56, s56, 0x8000
	v_or_b32_sdwa v17, v17, v23 dst_sel:DWORD dst_unused:UNUSED_PAD src0_sel:DWORD src1_sel:WORD_1
	v_or_b32_sdwa v16, v16, v22 dst_sel:DWORD dst_unused:UNUSED_PAD src0_sel:DWORD src1_sel:WORD_1
	s_addc_u32 s57, s57, 0
	global_store_dwordx2 v[26:27], v[16:17], off offset:3104
	v_add_u32_e32 v29, 0x200, v29
	s_waitcnt vmcnt(14)
	v_add_u32_e32 v28, -16, v29
	ds_read_b128 v[30:33], v28
	ds_read_b128 v[34:37], v29
	s_mov_b32 s58, 0x800000
	s_waitcnt lgkmcnt(1)
	v_mov_b32_e32 v38, v31
	v_mov_b32_e32 v39, v32
	v_mov_b32_e32 v31, v33
	v_pk_add_f32 v[30:31], v[38:39], v[30:31]
	s_waitcnt lgkmcnt(0)
	v_mov_b32_e32 v32, v36
	v_mov_b32_e32 v33, v34
	v_mov_b32_e32 v34, v37
	v_pk_add_f32 v[32:33], v[32:33], v[34:35]
	v_add_f32_e32 v28, v30, v31
	v_add_f32_e32 v28, v28, v33
	v_add_f32_e32 v28, v32, v28
	v_fmamk_f32 v28, v28, 0x3b800000, v195
	v_cmp_gt_f32_e32 vcc, s58, v28
	v_mul_f32_e32 v30, 0x4b800000, v28
	v_lshlrev_b32_e32 v33, 16, v43
	v_cndmask_b32_e32 v28, v28, v30, vcc
	v_rsq_f32_e32 v28, v28
	v_lshlrev_b32_e32 v32, 16, v42
	v_and_b32_e32 v43, 0xffff0000, v43
	v_and_b32_e32 v42, 0xffff0000, v42
	v_mul_f32_e32 v30, 0x45800000, v28
	v_cndmask_b32_e32 v28, v28, v30, vcc
	v_pk_mul_f32 v[32:33], v[28:29], v[32:33] op_sel_hi:[0,1]
	v_pk_mul_f32 v[32:33], v[0:1], v[32:33]
	v_lshlrev_b32_e32 v35, 16, v41
	v_lshlrev_b32_e32 v34, 16, v40
	v_pk_mul_f32 v[42:43], v[28:29], v[42:43] op_sel_hi:[0,1]
	v_pk_mul_f32 v[32:33], v[32:33], v[34:35]
	v_pk_mul_f32 v[42:43], v[8:9], v[42:43]
	v_and_b32_e32 v41, 0xffff0000, v41
	v_and_b32_e32 v40, 0xffff0000, v40
	v_pk_mul_f32 v[40:41], v[42:43], v[40:41]
	v_and_b32_sdwa v43, v32, v198 dst_sel:DWORD dst_unused:UNUSED_PAD src0_sel:WORD_1 src1_sel:DWORD
	v_and_b32_sdwa v42, v33, v198 dst_sel:DWORD dst_unused:UNUSED_PAD src0_sel:WORD_1 src1_sel:DWORD
	v_add3_u32 v43, v32, v43, s71
	v_and_b32_sdwa v32, v41, v198 dst_sel:DWORD dst_unused:UNUSED_PAD src0_sel:WORD_1 src1_sel:DWORD
	v_add3_u32 v42, v33, v42, s71
	v_and_b32_sdwa v33, v40, v198 dst_sel:DWORD dst_unused:UNUSED_PAD src0_sel:WORD_1 src1_sel:DWORD
	v_add3_u32 v41, v41, v32, s71
	v_lshl_add_u64 v[30:31], v[10:11], 0, s[56:57]
	v_add3_u32 v40, v40, v33, s71
	v_and_b32_e32 v41, 0xffff0000, v41
	v_and_b32_e32 v40, 0xffff0000, v40
	v_or_b32_sdwa v41, v41, v42 dst_sel:DWORD dst_unused:UNUSED_PAD src0_sel:DWORD src1_sel:WORD_1
	v_add_co_u32_e32 v42, vcc, s72, v30
	v_or_b32_sdwa v40, v40, v43 dst_sel:DWORD dst_unused:UNUSED_PAD src0_sel:DWORD src1_sel:WORD_1
	s_nop 0
	v_addc_co_u32_e32 v43, vcc, 0, v31, vcc
	global_store_dwordx2 v[42:43], v[40:41], off offset:3072
	v_lshlrev_b32_e32 v41, 16, v47
	v_lshlrev_b32_e32 v40, 16, v46
	v_pk_mul_f32 v[40:41], v[28:29], v[40:41] op_sel_hi:[0,1]
	v_and_b32_e32 v47, 0xffff0000, v47
	v_and_b32_e32 v46, 0xffff0000, v46
	v_pk_mul_f32 v[40:41], v[4:5], v[40:41]
	v_lshlrev_b32_e32 v31, 16, v45
	v_lshlrev_b32_e32 v30, 16, v44
	v_pk_mul_f32 v[46:47], v[28:29], v[46:47] op_sel_hi:[0,1]
	v_pk_mul_f32 v[40:41], v[40:41], v[30:31]
	v_pk_mul_f32 v[46:47], v[2:3], v[46:47]
	v_and_b32_e32 v45, 0xffff0000, v45
	v_and_b32_e32 v44, 0xffff0000, v44
	v_pk_mul_f32 v[44:45], v[46:47], v[44:45]
	v_and_b32_sdwa v46, v41, v198 dst_sel:DWORD dst_unused:UNUSED_PAD src0_sel:WORD_1 src1_sel:DWORD
	v_and_b32_sdwa v47, v40, v198 dst_sel:DWORD dst_unused:UNUSED_PAD src0_sel:WORD_1 src1_sel:DWORD
	v_add3_u32 v40, v40, v47, s71
	v_add3_u32 v41, v41, v46, s71
	v_and_b32_sdwa v46, v45, v198 dst_sel:DWORD dst_unused:UNUSED_PAD src0_sel:WORD_1 src1_sel:DWORD
	v_and_b32_sdwa v47, v44, v198 dst_sel:DWORD dst_unused:UNUSED_PAD src0_sel:WORD_1 src1_sel:DWORD
	v_add3_u32 v45, v45, v46, s71
	v_add3_u32 v44, v44, v47, s71
	v_and_b32_e32 v45, 0xffff0000, v45
	v_and_b32_e32 v44, 0xffff0000, v44
	s_add_u32 s56, s56, 0x8000
	v_or_b32_sdwa v45, v45, v41 dst_sel:DWORD dst_unused:UNUSED_PAD src0_sel:DWORD src1_sel:WORD_1
	v_or_b32_sdwa v44, v44, v40 dst_sel:DWORD dst_unused:UNUSED_PAD src0_sel:DWORD src1_sel:WORD_1
	s_addc_u32 s57, s57, 0
	global_store_dwordx2 v[42:43], v[44:45], off offset:3104
	v_add_u32_e32 v29, 0x200, v29
	s_waitcnt vmcnt(14)
	v_add_u32_e32 v28, -16, v29
	ds_read_b128 v[30:33], v28
	ds_read_b128 v[34:37], v29
	s_mov_b32 s58, 0x800000
	s_waitcnt lgkmcnt(1)
	v_mov_b32_e32 v38, v31
	v_mov_b32_e32 v39, v32
	v_mov_b32_e32 v31, v33
	v_pk_add_f32 v[30:31], v[38:39], v[30:31]
	s_waitcnt lgkmcnt(0)
	v_mov_b32_e32 v32, v36
	v_mov_b32_e32 v33, v34
	v_mov_b32_e32 v34, v37
	v_pk_add_f32 v[32:33], v[32:33], v[34:35]
	v_add_f32_e32 v28, v30, v31
	v_add_f32_e32 v28, v28, v33
	v_add_f32_e32 v28, v32, v28
	v_fmamk_f32 v28, v28, 0x3b800000, v195
	v_cmp_gt_f32_e32 vcc, s58, v28
	v_mul_f32_e32 v30, 0x4b800000, v28
	v_lshlrev_b32_e32 v33, 16, v51
	v_cndmask_b32_e32 v28, v28, v30, vcc
	v_rsq_f32_e32 v28, v28
	v_lshlrev_b32_e32 v32, 16, v50
	v_and_b32_e32 v51, 0xffff0000, v51
	v_and_b32_e32 v50, 0xffff0000, v50
	v_mul_f32_e32 v30, 0x45800000, v28
	v_cndmask_b32_e32 v28, v28, v30, vcc
	v_pk_mul_f32 v[32:33], v[28:29], v[32:33] op_sel_hi:[0,1]
	v_pk_mul_f32 v[32:33], v[0:1], v[32:33]
	v_lshlrev_b32_e32 v35, 16, v49
	v_lshlrev_b32_e32 v34, 16, v48
	v_pk_mul_f32 v[50:51], v[28:29], v[50:51] op_sel_hi:[0,1]
	v_pk_mul_f32 v[32:33], v[32:33], v[34:35]
	v_pk_mul_f32 v[50:51], v[8:9], v[50:51]
	v_and_b32_e32 v49, 0xffff0000, v49
	v_and_b32_e32 v48, 0xffff0000, v48
	v_pk_mul_f32 v[48:49], v[50:51], v[48:49]
	v_and_b32_sdwa v51, v32, v198 dst_sel:DWORD dst_unused:UNUSED_PAD src0_sel:WORD_1 src1_sel:DWORD
	v_and_b32_sdwa v50, v33, v198 dst_sel:DWORD dst_unused:UNUSED_PAD src0_sel:WORD_1 src1_sel:DWORD
	v_add3_u32 v51, v32, v51, s71
	v_and_b32_sdwa v32, v49, v198 dst_sel:DWORD dst_unused:UNUSED_PAD src0_sel:WORD_1 src1_sel:DWORD
	v_add3_u32 v50, v33, v50, s71
	v_and_b32_sdwa v33, v48, v198 dst_sel:DWORD dst_unused:UNUSED_PAD src0_sel:WORD_1 src1_sel:DWORD
	v_add3_u32 v49, v49, v32, s71
	v_lshl_add_u64 v[30:31], v[10:11], 0, s[56:57]
	v_add3_u32 v48, v48, v33, s71
	v_and_b32_e32 v49, 0xffff0000, v49
	v_and_b32_e32 v48, 0xffff0000, v48
	v_or_b32_sdwa v49, v49, v50 dst_sel:DWORD dst_unused:UNUSED_PAD src0_sel:DWORD src1_sel:WORD_1
	v_add_co_u32_e32 v50, vcc, s72, v30
	v_or_b32_sdwa v48, v48, v51 dst_sel:DWORD dst_unused:UNUSED_PAD src0_sel:DWORD src1_sel:WORD_1
	s_nop 0
	v_addc_co_u32_e32 v51, vcc, 0, v31, vcc
	global_store_dwordx2 v[50:51], v[48:49], off offset:3072
	v_lshlrev_b32_e32 v49, 16, v55
	v_lshlrev_b32_e32 v48, 16, v54
	v_pk_mul_f32 v[48:49], v[28:29], v[48:49] op_sel_hi:[0,1]
	v_and_b32_e32 v55, 0xffff0000, v55
	v_and_b32_e32 v54, 0xffff0000, v54
	v_pk_mul_f32 v[48:49], v[4:5], v[48:49]
	v_lshlrev_b32_e32 v31, 16, v53
	v_lshlrev_b32_e32 v30, 16, v52
	v_pk_mul_f32 v[54:55], v[28:29], v[54:55] op_sel_hi:[0,1]
	v_pk_mul_f32 v[48:49], v[48:49], v[30:31]
	v_pk_mul_f32 v[54:55], v[2:3], v[54:55]
	v_and_b32_e32 v53, 0xffff0000, v53
	v_and_b32_e32 v52, 0xffff0000, v52
	v_pk_mul_f32 v[52:53], v[54:55], v[52:53]
	v_and_b32_sdwa v54, v49, v198 dst_sel:DWORD dst_unused:UNUSED_PAD src0_sel:WORD_1 src1_sel:DWORD
	v_and_b32_sdwa v55, v48, v198 dst_sel:DWORD dst_unused:UNUSED_PAD src0_sel:WORD_1 src1_sel:DWORD
	v_add3_u32 v48, v48, v55, s71
	v_add3_u32 v49, v49, v54, s71
	v_and_b32_sdwa v54, v53, v198 dst_sel:DWORD dst_unused:UNUSED_PAD src0_sel:WORD_1 src1_sel:DWORD
	v_and_b32_sdwa v55, v52, v198 dst_sel:DWORD dst_unused:UNUSED_PAD src0_sel:WORD_1 src1_sel:DWORD
	v_add3_u32 v53, v53, v54, s71
	v_add3_u32 v52, v52, v55, s71
	v_and_b32_e32 v53, 0xffff0000, v53
	v_and_b32_e32 v52, 0xffff0000, v52
	s_add_u32 s56, s56, 0x8000
	v_or_b32_sdwa v53, v53, v49 dst_sel:DWORD dst_unused:UNUSED_PAD src0_sel:DWORD src1_sel:WORD_1
	v_or_b32_sdwa v52, v52, v48 dst_sel:DWORD dst_unused:UNUSED_PAD src0_sel:DWORD src1_sel:WORD_1
	s_addc_u32 s57, s57, 0
	global_store_dwordx2 v[50:51], v[52:53], off offset:3104
	v_add_u32_e32 v29, 0x200, v29
	s_waitcnt vmcnt(14)
	v_add_u32_e32 v28, -16, v29
	ds_read_b128 v[30:33], v28
	ds_read_b128 v[34:37], v29
	s_mov_b32 s58, 0x800000
	s_waitcnt lgkmcnt(1)
	v_mov_b32_e32 v38, v31
	v_mov_b32_e32 v39, v32
	v_mov_b32_e32 v31, v33
	v_pk_add_f32 v[30:31], v[38:39], v[30:31]
	s_waitcnt lgkmcnt(0)
	v_mov_b32_e32 v32, v36
	v_mov_b32_e32 v33, v34
	v_mov_b32_e32 v34, v37
	v_pk_add_f32 v[32:33], v[32:33], v[34:35]
	v_add_f32_e32 v28, v30, v31
	v_add_f32_e32 v28, v28, v33
	v_add_f32_e32 v28, v32, v28
	v_fmamk_f32 v28, v28, 0x3b800000, v195
	v_cmp_gt_f32_e32 vcc, s58, v28
	v_mul_f32_e32 v30, 0x4b800000, v28
	v_lshlrev_b32_e32 v33, 16, v59
	v_cndmask_b32_e32 v28, v28, v30, vcc
	v_rsq_f32_e32 v28, v28
	v_lshlrev_b32_e32 v32, 16, v58
	v_and_b32_e32 v59, 0xffff0000, v59
	v_and_b32_e32 v58, 0xffff0000, v58
	v_mul_f32_e32 v30, 0x45800000, v28
	v_cndmask_b32_e32 v28, v28, v30, vcc
	v_pk_mul_f32 v[32:33], v[28:29], v[32:33] op_sel_hi:[0,1]
	v_pk_mul_f32 v[32:33], v[0:1], v[32:33]
	v_lshlrev_b32_e32 v35, 16, v57
	v_lshlrev_b32_e32 v34, 16, v56
	v_pk_mul_f32 v[58:59], v[28:29], v[58:59] op_sel_hi:[0,1]
	v_pk_mul_f32 v[32:33], v[32:33], v[34:35]
	v_pk_mul_f32 v[58:59], v[8:9], v[58:59]
	v_and_b32_e32 v57, 0xffff0000, v57
	v_and_b32_e32 v56, 0xffff0000, v56
	v_pk_mul_f32 v[56:57], v[58:59], v[56:57]
	v_and_b32_sdwa v59, v32, v198 dst_sel:DWORD dst_unused:UNUSED_PAD src0_sel:WORD_1 src1_sel:DWORD
	v_and_b32_sdwa v58, v33, v198 dst_sel:DWORD dst_unused:UNUSED_PAD src0_sel:WORD_1 src1_sel:DWORD
	v_add3_u32 v59, v32, v59, s71
	v_and_b32_sdwa v32, v57, v198 dst_sel:DWORD dst_unused:UNUSED_PAD src0_sel:WORD_1 src1_sel:DWORD
	v_add3_u32 v58, v33, v58, s71
	v_and_b32_sdwa v33, v56, v198 dst_sel:DWORD dst_unused:UNUSED_PAD src0_sel:WORD_1 src1_sel:DWORD
	v_add3_u32 v57, v57, v32, s71
	v_lshl_add_u64 v[30:31], v[10:11], 0, s[56:57]
	v_add3_u32 v56, v56, v33, s71
	v_and_b32_e32 v57, 0xffff0000, v57
	v_and_b32_e32 v56, 0xffff0000, v56
	v_or_b32_sdwa v57, v57, v58 dst_sel:DWORD dst_unused:UNUSED_PAD src0_sel:DWORD src1_sel:WORD_1
	v_add_co_u32_e32 v58, vcc, s72, v30
	v_or_b32_sdwa v56, v56, v59 dst_sel:DWORD dst_unused:UNUSED_PAD src0_sel:DWORD src1_sel:WORD_1
	s_nop 0
	v_addc_co_u32_e32 v59, vcc, 0, v31, vcc
	global_store_dwordx2 v[58:59], v[56:57], off offset:3072
	v_lshlrev_b32_e32 v57, 16, v63
	v_lshlrev_b32_e32 v56, 16, v62
	v_pk_mul_f32 v[56:57], v[28:29], v[56:57] op_sel_hi:[0,1]
	v_and_b32_e32 v63, 0xffff0000, v63
	v_and_b32_e32 v62, 0xffff0000, v62
	v_pk_mul_f32 v[56:57], v[4:5], v[56:57]
	v_lshlrev_b32_e32 v31, 16, v61
	v_lshlrev_b32_e32 v30, 16, v60
	v_pk_mul_f32 v[62:63], v[28:29], v[62:63] op_sel_hi:[0,1]
	v_pk_mul_f32 v[56:57], v[56:57], v[30:31]
	v_pk_mul_f32 v[62:63], v[2:3], v[62:63]
	v_and_b32_e32 v61, 0xffff0000, v61
	v_and_b32_e32 v60, 0xffff0000, v60
	v_pk_mul_f32 v[60:61], v[62:63], v[60:61]
	v_and_b32_sdwa v62, v57, v198 dst_sel:DWORD dst_unused:UNUSED_PAD src0_sel:WORD_1 src1_sel:DWORD
	v_and_b32_sdwa v63, v56, v198 dst_sel:DWORD dst_unused:UNUSED_PAD src0_sel:WORD_1 src1_sel:DWORD
	v_add3_u32 v56, v56, v63, s71
	v_add3_u32 v57, v57, v62, s71
	v_and_b32_sdwa v62, v61, v198 dst_sel:DWORD dst_unused:UNUSED_PAD src0_sel:WORD_1 src1_sel:DWORD
	v_and_b32_sdwa v63, v60, v198 dst_sel:DWORD dst_unused:UNUSED_PAD src0_sel:WORD_1 src1_sel:DWORD
	v_add3_u32 v61, v61, v62, s71
	v_add3_u32 v60, v60, v63, s71
	v_and_b32_e32 v61, 0xffff0000, v61
	v_and_b32_e32 v60, 0xffff0000, v60
	s_add_u32 s56, s56, 0x8000
	v_or_b32_sdwa v61, v61, v57 dst_sel:DWORD dst_unused:UNUSED_PAD src0_sel:DWORD src1_sel:WORD_1
	v_or_b32_sdwa v60, v60, v56 dst_sel:DWORD dst_unused:UNUSED_PAD src0_sel:DWORD src1_sel:WORD_1
	s_addc_u32 s57, s57, 0
	global_store_dwordx2 v[58:59], v[60:61], off offset:3104
	v_add_u32_e32 v29, 0x200, v29
	s_waitcnt vmcnt(14)
	v_add_u32_e32 v28, -16, v29
	ds_read_b128 v[30:33], v28
	ds_read_b128 v[34:37], v29
	s_mov_b32 s58, 0x800000
	s_waitcnt lgkmcnt(1)
	v_mov_b32_e32 v38, v31
	v_mov_b32_e32 v39, v32
	v_mov_b32_e32 v31, v33
	v_pk_add_f32 v[30:31], v[38:39], v[30:31]
	s_waitcnt lgkmcnt(0)
	v_mov_b32_e32 v32, v36
	v_mov_b32_e32 v33, v34
	v_mov_b32_e32 v34, v37
	v_pk_add_f32 v[32:33], v[32:33], v[34:35]
	v_add_f32_e32 v28, v30, v31
	v_add_f32_e32 v28, v28, v33
	v_add_f32_e32 v28, v32, v28
	v_fmamk_f32 v28, v28, 0x3b800000, v195
	v_cmp_gt_f32_e32 vcc, s58, v28
	v_mul_f32_e32 v30, 0x4b800000, v28
	v_lshlrev_b32_e32 v33, 16, v67
	v_cndmask_b32_e32 v28, v28, v30, vcc
	v_rsq_f32_e32 v28, v28
	v_lshlrev_b32_e32 v32, 16, v66
	v_and_b32_e32 v67, 0xffff0000, v67
	v_and_b32_e32 v66, 0xffff0000, v66
	v_mul_f32_e32 v30, 0x45800000, v28
	v_cndmask_b32_e32 v28, v28, v30, vcc
	v_pk_mul_f32 v[32:33], v[28:29], v[32:33] op_sel_hi:[0,1]
	v_pk_mul_f32 v[32:33], v[0:1], v[32:33]
	v_lshlrev_b32_e32 v35, 16, v65
	v_lshlrev_b32_e32 v34, 16, v64
	v_pk_mul_f32 v[66:67], v[28:29], v[66:67] op_sel_hi:[0,1]
	v_pk_mul_f32 v[32:33], v[32:33], v[34:35]
	v_pk_mul_f32 v[66:67], v[8:9], v[66:67]
	v_and_b32_e32 v65, 0xffff0000, v65
	v_and_b32_e32 v64, 0xffff0000, v64
	v_pk_mul_f32 v[64:65], v[66:67], v[64:65]
	v_and_b32_sdwa v67, v32, v198 dst_sel:DWORD dst_unused:UNUSED_PAD src0_sel:WORD_1 src1_sel:DWORD
	v_and_b32_sdwa v66, v33, v198 dst_sel:DWORD dst_unused:UNUSED_PAD src0_sel:WORD_1 src1_sel:DWORD
	v_add3_u32 v67, v32, v67, s71
	v_and_b32_sdwa v32, v65, v198 dst_sel:DWORD dst_unused:UNUSED_PAD src0_sel:WORD_1 src1_sel:DWORD
	v_add3_u32 v66, v33, v66, s71
	v_and_b32_sdwa v33, v64, v198 dst_sel:DWORD dst_unused:UNUSED_PAD src0_sel:WORD_1 src1_sel:DWORD
	v_add3_u32 v65, v65, v32, s71
	v_lshl_add_u64 v[30:31], v[10:11], 0, s[56:57]
	v_add3_u32 v64, v64, v33, s71
	v_and_b32_e32 v65, 0xffff0000, v65
	v_and_b32_e32 v64, 0xffff0000, v64
	v_or_b32_sdwa v65, v65, v66 dst_sel:DWORD dst_unused:UNUSED_PAD src0_sel:DWORD src1_sel:WORD_1
	v_add_co_u32_e32 v66, vcc, s72, v30
	v_or_b32_sdwa v64, v64, v67 dst_sel:DWORD dst_unused:UNUSED_PAD src0_sel:DWORD src1_sel:WORD_1
	s_nop 0
	v_addc_co_u32_e32 v67, vcc, 0, v31, vcc
	global_store_dwordx2 v[66:67], v[64:65], off offset:3072
	v_lshlrev_b32_e32 v65, 16, v71
	v_lshlrev_b32_e32 v64, 16, v70
	v_pk_mul_f32 v[64:65], v[28:29], v[64:65] op_sel_hi:[0,1]
	v_and_b32_e32 v71, 0xffff0000, v71
	v_and_b32_e32 v70, 0xffff0000, v70
	v_pk_mul_f32 v[64:65], v[4:5], v[64:65]
	v_lshlrev_b32_e32 v31, 16, v69
	v_lshlrev_b32_e32 v30, 16, v68
	v_pk_mul_f32 v[70:71], v[28:29], v[70:71] op_sel_hi:[0,1]
	v_pk_mul_f32 v[64:65], v[64:65], v[30:31]
	v_pk_mul_f32 v[70:71], v[2:3], v[70:71]
	v_and_b32_e32 v69, 0xffff0000, v69
	v_and_b32_e32 v68, 0xffff0000, v68
	v_pk_mul_f32 v[68:69], v[70:71], v[68:69]
	v_and_b32_sdwa v70, v65, v198 dst_sel:DWORD dst_unused:UNUSED_PAD src0_sel:WORD_1 src1_sel:DWORD
	v_and_b32_sdwa v71, v64, v198 dst_sel:DWORD dst_unused:UNUSED_PAD src0_sel:WORD_1 src1_sel:DWORD
	v_add3_u32 v64, v64, v71, s71
	v_add3_u32 v65, v65, v70, s71
	v_and_b32_sdwa v70, v69, v198 dst_sel:DWORD dst_unused:UNUSED_PAD src0_sel:WORD_1 src1_sel:DWORD
	v_and_b32_sdwa v71, v68, v198 dst_sel:DWORD dst_unused:UNUSED_PAD src0_sel:WORD_1 src1_sel:DWORD
	v_add3_u32 v69, v69, v70, s71
	v_add3_u32 v68, v68, v71, s71
	v_and_b32_e32 v69, 0xffff0000, v69
	v_and_b32_e32 v68, 0xffff0000, v68
	s_add_u32 s56, s56, 0x8000
	v_or_b32_sdwa v69, v69, v65 dst_sel:DWORD dst_unused:UNUSED_PAD src0_sel:DWORD src1_sel:WORD_1
	v_or_b32_sdwa v68, v68, v64 dst_sel:DWORD dst_unused:UNUSED_PAD src0_sel:DWORD src1_sel:WORD_1
	s_addc_u32 s57, s57, 0
	global_store_dwordx2 v[66:67], v[68:69], off offset:3104
	v_add_u32_e32 v29, 0x200, v29
	s_waitcnt vmcnt(14)
	v_add_u32_e32 v28, -16, v29
	ds_read_b128 v[30:33], v28
	ds_read_b128 v[34:37], v29
	s_mov_b32 s58, 0x800000
	s_waitcnt lgkmcnt(1)
	v_mov_b32_e32 v38, v31
	v_mov_b32_e32 v39, v32
	v_mov_b32_e32 v31, v33
	v_pk_add_f32 v[30:31], v[38:39], v[30:31]
	s_waitcnt lgkmcnt(0)
	v_mov_b32_e32 v32, v36
	v_mov_b32_e32 v33, v34
	v_mov_b32_e32 v34, v37
	v_pk_add_f32 v[32:33], v[32:33], v[34:35]
	v_add_f32_e32 v28, v30, v31
	v_add_f32_e32 v28, v28, v33
	v_add_f32_e32 v28, v32, v28
	v_fmamk_f32 v28, v28, 0x3b800000, v195
	v_cmp_gt_f32_e32 vcc, s58, v28
	v_mul_f32_e32 v30, 0x4b800000, v28
	v_lshlrev_b32_e32 v33, 16, v75
	v_cndmask_b32_e32 v28, v28, v30, vcc
	v_rsq_f32_e32 v28, v28
	v_lshlrev_b32_e32 v32, 16, v74
	v_and_b32_e32 v75, 0xffff0000, v75
	v_and_b32_e32 v74, 0xffff0000, v74
	v_mul_f32_e32 v30, 0x45800000, v28
	v_cndmask_b32_e32 v28, v28, v30, vcc
	v_pk_mul_f32 v[32:33], v[28:29], v[32:33] op_sel_hi:[0,1]
	v_pk_mul_f32 v[32:33], v[0:1], v[32:33]
	v_lshlrev_b32_e32 v35, 16, v73
	v_lshlrev_b32_e32 v34, 16, v72
	v_pk_mul_f32 v[74:75], v[28:29], v[74:75] op_sel_hi:[0,1]
	v_pk_mul_f32 v[32:33], v[32:33], v[34:35]
	v_pk_mul_f32 v[74:75], v[8:9], v[74:75]
	v_and_b32_e32 v73, 0xffff0000, v73
	v_and_b32_e32 v72, 0xffff0000, v72
	v_pk_mul_f32 v[72:73], v[74:75], v[72:73]
	v_and_b32_sdwa v75, v32, v198 dst_sel:DWORD dst_unused:UNUSED_PAD src0_sel:WORD_1 src1_sel:DWORD
	v_and_b32_sdwa v74, v33, v198 dst_sel:DWORD dst_unused:UNUSED_PAD src0_sel:WORD_1 src1_sel:DWORD
	v_add3_u32 v75, v32, v75, s71
	v_and_b32_sdwa v32, v73, v198 dst_sel:DWORD dst_unused:UNUSED_PAD src0_sel:WORD_1 src1_sel:DWORD
	v_add3_u32 v74, v33, v74, s71
	v_and_b32_sdwa v33, v72, v198 dst_sel:DWORD dst_unused:UNUSED_PAD src0_sel:WORD_1 src1_sel:DWORD
	v_add3_u32 v73, v73, v32, s71
	v_lshl_add_u64 v[30:31], v[10:11], 0, s[56:57]
	v_add3_u32 v72, v72, v33, s71
	v_and_b32_e32 v73, 0xffff0000, v73
	v_and_b32_e32 v72, 0xffff0000, v72
	v_or_b32_sdwa v73, v73, v74 dst_sel:DWORD dst_unused:UNUSED_PAD src0_sel:DWORD src1_sel:WORD_1
	v_add_co_u32_e32 v74, vcc, s72, v30
	v_or_b32_sdwa v72, v72, v75 dst_sel:DWORD dst_unused:UNUSED_PAD src0_sel:DWORD src1_sel:WORD_1
	s_nop 0
	v_addc_co_u32_e32 v75, vcc, 0, v31, vcc
	global_store_dwordx2 v[74:75], v[72:73], off offset:3072
	v_lshlrev_b32_e32 v73, 16, v79
	v_lshlrev_b32_e32 v72, 16, v78
	v_pk_mul_f32 v[72:73], v[28:29], v[72:73] op_sel_hi:[0,1]
	v_and_b32_e32 v79, 0xffff0000, v79
	v_and_b32_e32 v78, 0xffff0000, v78
	v_pk_mul_f32 v[72:73], v[4:5], v[72:73]
	v_lshlrev_b32_e32 v31, 16, v77
	v_lshlrev_b32_e32 v30, 16, v76
	v_pk_mul_f32 v[78:79], v[28:29], v[78:79] op_sel_hi:[0,1]
	v_pk_mul_f32 v[72:73], v[72:73], v[30:31]
	v_pk_mul_f32 v[78:79], v[2:3], v[78:79]
	v_and_b32_e32 v77, 0xffff0000, v77
	v_and_b32_e32 v76, 0xffff0000, v76
	v_pk_mul_f32 v[76:77], v[78:79], v[76:77]
	v_and_b32_sdwa v78, v73, v198 dst_sel:DWORD dst_unused:UNUSED_PAD src0_sel:WORD_1 src1_sel:DWORD
	v_and_b32_sdwa v79, v72, v198 dst_sel:DWORD dst_unused:UNUSED_PAD src0_sel:WORD_1 src1_sel:DWORD
	v_add3_u32 v72, v72, v79, s71
	v_add3_u32 v73, v73, v78, s71
	v_and_b32_sdwa v78, v77, v198 dst_sel:DWORD dst_unused:UNUSED_PAD src0_sel:WORD_1 src1_sel:DWORD
	v_and_b32_sdwa v79, v76, v198 dst_sel:DWORD dst_unused:UNUSED_PAD src0_sel:WORD_1 src1_sel:DWORD
	v_add3_u32 v77, v77, v78, s71
	v_add3_u32 v76, v76, v79, s71
	v_and_b32_e32 v77, 0xffff0000, v77
	v_and_b32_e32 v76, 0xffff0000, v76
	s_add_u32 s56, s56, 0x8000
	v_or_b32_sdwa v77, v77, v73 dst_sel:DWORD dst_unused:UNUSED_PAD src0_sel:DWORD src1_sel:WORD_1
	v_or_b32_sdwa v76, v76, v72 dst_sel:DWORD dst_unused:UNUSED_PAD src0_sel:DWORD src1_sel:WORD_1
	s_addc_u32 s57, s57, 0
	global_store_dwordx2 v[74:75], v[76:77], off offset:3104
	v_add_u32_e32 v29, 0x200, v29
	s_waitcnt vmcnt(14)
	v_add_u32_e32 v28, -16, v29
	ds_read_b128 v[30:33], v28
	ds_read_b128 v[34:37], v29
	s_mov_b32 s58, 0x800000
	s_waitcnt lgkmcnt(1)
	v_mov_b32_e32 v38, v31
	v_mov_b32_e32 v39, v32
	v_mov_b32_e32 v31, v33
	v_pk_add_f32 v[30:31], v[38:39], v[30:31]
	s_waitcnt lgkmcnt(0)
	v_mov_b32_e32 v32, v36
	v_mov_b32_e32 v33, v34
	v_mov_b32_e32 v34, v37
	v_pk_add_f32 v[32:33], v[32:33], v[34:35]
	v_add_f32_e32 v28, v30, v31
	v_add_f32_e32 v28, v28, v33
	v_add_f32_e32 v28, v32, v28
	v_fmamk_f32 v28, v28, 0x3b800000, v195
	v_cmp_gt_f32_e32 vcc, s58, v28
	v_mul_f32_e32 v30, 0x4b800000, v28
	v_lshlrev_b32_e32 v33, 16, v203
	v_cndmask_b32_e32 v28, v28, v30, vcc
	v_rsq_f32_e32 v28, v28
	v_lshlrev_b32_e32 v32, 16, v202
	v_and_b32_e32 v203, 0xffff0000, v203
	v_and_b32_e32 v202, 0xffff0000, v202
	v_mul_f32_e32 v30, 0x45800000, v28
	v_cndmask_b32_e32 v28, v28, v30, vcc
	v_pk_mul_f32 v[32:33], v[28:29], v[32:33] op_sel_hi:[0,1]
	v_pk_mul_f32 v[32:33], v[0:1], v[32:33]
	v_lshlrev_b32_e32 v35, 16, v201
	v_lshlrev_b32_e32 v34, 16, v200
	v_pk_mul_f32 v[202:203], v[28:29], v[202:203] op_sel_hi:[0,1]
	v_pk_mul_f32 v[32:33], v[32:33], v[34:35]
	v_pk_mul_f32 v[202:203], v[8:9], v[202:203]
	v_and_b32_e32 v201, 0xffff0000, v201
	v_and_b32_e32 v200, 0xffff0000, v200
	v_pk_mul_f32 v[200:201], v[202:203], v[200:201]
	v_and_b32_sdwa v203, v32, v198 dst_sel:DWORD dst_unused:UNUSED_PAD src0_sel:WORD_1 src1_sel:DWORD
	v_and_b32_sdwa v202, v33, v198 dst_sel:DWORD dst_unused:UNUSED_PAD src0_sel:WORD_1 src1_sel:DWORD
	v_add3_u32 v203, v32, v203, s71
	v_and_b32_sdwa v32, v201, v198 dst_sel:DWORD dst_unused:UNUSED_PAD src0_sel:WORD_1 src1_sel:DWORD
	v_add3_u32 v202, v33, v202, s71
	v_and_b32_sdwa v33, v200, v198 dst_sel:DWORD dst_unused:UNUSED_PAD src0_sel:WORD_1 src1_sel:DWORD
	v_add3_u32 v201, v201, v32, s71
	v_lshl_add_u64 v[30:31], v[10:11], 0, s[56:57]
	v_add3_u32 v200, v200, v33, s71
	v_and_b32_e32 v201, 0xffff0000, v201
	v_and_b32_e32 v200, 0xffff0000, v200
	v_or_b32_sdwa v201, v201, v202 dst_sel:DWORD dst_unused:UNUSED_PAD src0_sel:DWORD src1_sel:WORD_1
	v_add_co_u32_e32 v202, vcc, s72, v30
	v_or_b32_sdwa v200, v200, v203 dst_sel:DWORD dst_unused:UNUSED_PAD src0_sel:DWORD src1_sel:WORD_1
	s_nop 0
	v_addc_co_u32_e32 v203, vcc, 0, v31, vcc
	global_store_dwordx2 v[202:203], v[200:201], off offset:3072
	v_lshlrev_b32_e32 v201, 16, v207
	v_lshlrev_b32_e32 v200, 16, v206
	v_pk_mul_f32 v[200:201], v[28:29], v[200:201] op_sel_hi:[0,1]
	v_and_b32_e32 v207, 0xffff0000, v207
	v_and_b32_e32 v206, 0xffff0000, v206
	v_pk_mul_f32 v[200:201], v[4:5], v[200:201]
	v_lshlrev_b32_e32 v31, 16, v205
	v_lshlrev_b32_e32 v30, 16, v204
	v_pk_mul_f32 v[206:207], v[28:29], v[206:207] op_sel_hi:[0,1]
	v_pk_mul_f32 v[200:201], v[200:201], v[30:31]
	v_pk_mul_f32 v[206:207], v[2:3], v[206:207]
	v_and_b32_e32 v205, 0xffff0000, v205
	v_and_b32_e32 v204, 0xffff0000, v204
	v_pk_mul_f32 v[204:205], v[206:207], v[204:205]
	v_and_b32_sdwa v206, v201, v198 dst_sel:DWORD dst_unused:UNUSED_PAD src0_sel:WORD_1 src1_sel:DWORD
	v_and_b32_sdwa v207, v200, v198 dst_sel:DWORD dst_unused:UNUSED_PAD src0_sel:WORD_1 src1_sel:DWORD
	v_add3_u32 v200, v200, v207, s71
	v_add3_u32 v201, v201, v206, s71
	v_and_b32_sdwa v206, v205, v198 dst_sel:DWORD dst_unused:UNUSED_PAD src0_sel:WORD_1 src1_sel:DWORD
	v_and_b32_sdwa v207, v204, v198 dst_sel:DWORD dst_unused:UNUSED_PAD src0_sel:WORD_1 src1_sel:DWORD
	v_add3_u32 v205, v205, v206, s71
	v_add3_u32 v204, v204, v207, s71
	v_and_b32_e32 v205, 0xffff0000, v205
	v_and_b32_e32 v204, 0xffff0000, v204
	s_add_u32 s56, s56, 0x8000
	v_or_b32_sdwa v205, v205, v201 dst_sel:DWORD dst_unused:UNUSED_PAD src0_sel:DWORD src1_sel:WORD_1
	v_or_b32_sdwa v204, v204, v200 dst_sel:DWORD dst_unused:UNUSED_PAD src0_sel:DWORD src1_sel:WORD_1
	s_addc_u32 s57, s57, 0
	global_store_dwordx2 v[202:203], v[204:205], off offset:3104
	v_add_u32_e32 v29, 0x200, v29
	s_waitcnt vmcnt(14)
	v_add_u32_e32 v28, -16, v29
	ds_read_b128 v[30:33], v28
	ds_read_b128 v[34:37], v29
	s_mov_b32 s58, 0x800000
	s_waitcnt lgkmcnt(1)
	v_mov_b32_e32 v38, v31
	v_mov_b32_e32 v39, v32
	v_mov_b32_e32 v31, v33
	v_pk_add_f32 v[30:31], v[38:39], v[30:31]
	s_waitcnt lgkmcnt(0)
	v_mov_b32_e32 v32, v36
	v_mov_b32_e32 v33, v34
	v_mov_b32_e32 v34, v37
	v_pk_add_f32 v[32:33], v[32:33], v[34:35]
	v_add_f32_e32 v28, v30, v31
	v_add_f32_e32 v28, v28, v33
	v_add_f32_e32 v28, v32, v28
	v_fmamk_f32 v28, v28, 0x3b800000, v195
	v_cmp_gt_f32_e32 vcc, s58, v28
	v_mul_f32_e32 v30, 0x4b800000, v28
	v_lshlrev_b32_e32 v33, 16, v211
	v_cndmask_b32_e32 v28, v28, v30, vcc
	v_rsq_f32_e32 v28, v28
	v_lshlrev_b32_e32 v32, 16, v210
	v_and_b32_e32 v211, 0xffff0000, v211
	v_and_b32_e32 v210, 0xffff0000, v210
	v_mul_f32_e32 v30, 0x45800000, v28
	v_cndmask_b32_e32 v28, v28, v30, vcc
	v_pk_mul_f32 v[32:33], v[28:29], v[32:33] op_sel_hi:[0,1]
	v_pk_mul_f32 v[32:33], v[0:1], v[32:33]
	v_lshlrev_b32_e32 v35, 16, v209
	v_lshlrev_b32_e32 v34, 16, v208
	v_pk_mul_f32 v[210:211], v[28:29], v[210:211] op_sel_hi:[0,1]
	v_pk_mul_f32 v[32:33], v[32:33], v[34:35]
	v_pk_mul_f32 v[210:211], v[8:9], v[210:211]
	v_and_b32_e32 v209, 0xffff0000, v209
	v_and_b32_e32 v208, 0xffff0000, v208
	v_pk_mul_f32 v[208:209], v[210:211], v[208:209]
	v_and_b32_sdwa v211, v32, v198 dst_sel:DWORD dst_unused:UNUSED_PAD src0_sel:WORD_1 src1_sel:DWORD
	v_and_b32_sdwa v210, v33, v198 dst_sel:DWORD dst_unused:UNUSED_PAD src0_sel:WORD_1 src1_sel:DWORD
	v_add3_u32 v211, v32, v211, s71
	v_and_b32_sdwa v32, v209, v198 dst_sel:DWORD dst_unused:UNUSED_PAD src0_sel:WORD_1 src1_sel:DWORD
	v_add3_u32 v210, v33, v210, s71
	v_and_b32_sdwa v33, v208, v198 dst_sel:DWORD dst_unused:UNUSED_PAD src0_sel:WORD_1 src1_sel:DWORD
	v_add3_u32 v209, v209, v32, s71
	v_lshl_add_u64 v[30:31], v[10:11], 0, s[56:57]
	v_add3_u32 v208, v208, v33, s71
	v_and_b32_e32 v209, 0xffff0000, v209
	v_and_b32_e32 v208, 0xffff0000, v208
	v_or_b32_sdwa v209, v209, v210 dst_sel:DWORD dst_unused:UNUSED_PAD src0_sel:DWORD src1_sel:WORD_1
	v_add_co_u32_e32 v210, vcc, s72, v30
	v_or_b32_sdwa v208, v208, v211 dst_sel:DWORD dst_unused:UNUSED_PAD src0_sel:DWORD src1_sel:WORD_1
	s_nop 0
	v_addc_co_u32_e32 v211, vcc, 0, v31, vcc
	global_store_dwordx2 v[210:211], v[208:209], off offset:3072
	v_lshlrev_b32_e32 v209, 16, v215
	v_lshlrev_b32_e32 v208, 16, v214
	v_pk_mul_f32 v[208:209], v[28:29], v[208:209] op_sel_hi:[0,1]
	v_and_b32_e32 v215, 0xffff0000, v215
	v_and_b32_e32 v214, 0xffff0000, v214
	v_pk_mul_f32 v[208:209], v[4:5], v[208:209]
	v_lshlrev_b32_e32 v31, 16, v213
	v_lshlrev_b32_e32 v30, 16, v212
	v_pk_mul_f32 v[214:215], v[28:29], v[214:215] op_sel_hi:[0,1]
	v_pk_mul_f32 v[208:209], v[208:209], v[30:31]
	v_pk_mul_f32 v[214:215], v[2:3], v[214:215]
	v_and_b32_e32 v213, 0xffff0000, v213
	v_and_b32_e32 v212, 0xffff0000, v212
	v_pk_mul_f32 v[212:213], v[214:215], v[212:213]
	v_and_b32_sdwa v214, v209, v198 dst_sel:DWORD dst_unused:UNUSED_PAD src0_sel:WORD_1 src1_sel:DWORD
	v_and_b32_sdwa v215, v208, v198 dst_sel:DWORD dst_unused:UNUSED_PAD src0_sel:WORD_1 src1_sel:DWORD
	v_add3_u32 v208, v208, v215, s71
	v_add3_u32 v209, v209, v214, s71
	v_and_b32_sdwa v214, v213, v198 dst_sel:DWORD dst_unused:UNUSED_PAD src0_sel:WORD_1 src1_sel:DWORD
	v_and_b32_sdwa v215, v212, v198 dst_sel:DWORD dst_unused:UNUSED_PAD src0_sel:WORD_1 src1_sel:DWORD
	v_add3_u32 v213, v213, v214, s71
	v_add3_u32 v212, v212, v215, s71
	v_and_b32_e32 v213, 0xffff0000, v213
	v_and_b32_e32 v212, 0xffff0000, v212
	s_add_u32 s56, s56, 0x8000
	v_or_b32_sdwa v213, v213, v209 dst_sel:DWORD dst_unused:UNUSED_PAD src0_sel:DWORD src1_sel:WORD_1
	v_or_b32_sdwa v212, v212, v208 dst_sel:DWORD dst_unused:UNUSED_PAD src0_sel:DWORD src1_sel:WORD_1
	s_addc_u32 s57, s57, 0
	global_store_dwordx2 v[210:211], v[212:213], off offset:3104
	v_add_u32_e32 v29, 0x200, v29
	v_readlane_b32 s49, v253, 63
	s_add_i32 s52, s52, s49
	s_add_i32 s63, s63, s64
	s_cmpk_lt_i32 s52, 0x200
	s_barrier
	s_cbranch_scc1 .LBB0_759
	v_readlane_b32 s64, v253, 45
	v_readlane_b32 s48, v252, 16
	v_readlane_b32 s2, v252, 14
	v_readlane_b32 s68, v253, 49
	v_readlane_b32 s69, v253, 50
	v_readlane_b32 s72, v253, 53
	v_readlane_b32 s73, v253, 54
	v_readlane_b32 s84, v253, 63
	v_readlane_b32 s85, v252, 0
	v_readlane_b32 s86, v252, 1
	v_readlane_b32 s87, v252, 2
	v_readlane_b32 s90, v252, 3
	v_readlane_b32 s49, v252, 17
	v_readlane_b32 s3, v252, 15
	v_readlane_b32 s65, v253, 46
	v_readlane_b32 s66, v253, 47
	v_readlane_b32 s67, v253, 48
	v_readlane_b32 s70, v253, 51
	v_readlane_b32 s71, v253, 52
	v_readlane_b32 s74, v253, 55
	v_readlane_b32 s75, v253, 56
	v_readlane_b32 s76, v253, 57
	v_readlane_b32 s77, v253, 58
	v_readlane_b32 s78, v253, 59
	v_readlane_b32 s79, v253, 60
